# rows<3>: rank vectors fetched once per wave and broadcast, loop-top store drain and the mid-load wait removed, row data awaited at first read
# speedup vs baseline: 1.0038x; 1.0038x over previous
; DEVI float bflo(unsigned w) { return __uint_as_float(w << 16); }
; DEVI float bfhi(unsigned w) { return __uint_as_float(w & 0xffff0000u); }
; DEVI int obid() { int b = blockIdx.x; asm volatile("" : "+s"(b)); return b; }
; template <int MODE>
; DEVI void phase_rows(const Params& p, int l, char* smem) {
;     ...
;     const int nrows = (MODE == 3 || (MODE == 1 && l == 1)) ? NLAT : NROW;
;     for (int row = obid() * 8 + wid; row < nrows; row += gridDim.x * 8) {
;         const bool lat = row < NLAT;
;         const int b = lat ? (row >> 11) : ((row - NLAT) >> 8);
;         const int tok = lat ? (row & 2047) : (SEQ + ((row - NLAT) & 255));
;         float v[32];
;         if (MODE == 0) { const float* src = lat ? p.x + (size_t)row * DM : p.ctx + (size_t)(row - NLAT) * DM;
; #pragma unroll
;             for (int i = 0; i < 8; ++i) { const f32x4 t = *(const f32x4*)(src + i * 256 + lane * 4); v[i * 4] = t[0]; v[i * 4 + 1] = t[1]; v[i * 4 + 2] = t[2]; v[i * 4 + 3] = t[3]; }
;         } else { const bf16_t* src = xres + (size_t)row * DM;
; #pragma unroll
;             for (int i = 0; i < 8; ++i) { const u32x2 t = *(const u32x2*)(src + i * 256 + lane * 4); v[i * 4] = bflo(t[0]); v[i * 4 + 1] = bfhi(t[0]); v[i * 4 + 2] = bflo(t[1]); v[i * 4 + 3] = bfhi(t[1]); }
;         }
;         const float* mrow = mod + (size_t)(((MODE == 2) ? l : l) * 5 + (lat ? b : 4)) * 12288;
;         if (MODE == 2 || MODE == 3) {
;             float cacc[32];
; #pragma unroll
;             for (int i = 0; i < 32; ++i) cacc[i] = 0.f;
;             const int* rk = (const int*)(p.ws + WS_RANK) + (size_t)b * 16 * KEYS + tok;
;             const bf16_t* ydn = (const bf16_t*)(p.ws + WS_YDN);
;             const int cap = lat ? 256 : 32;
;             int rke[16];
; #pragma unroll
;             for (int e = 0; e < 16; ++e) rke[e] = rk[e * KEYS];
;             const bf16_t* y0 = ydn; const bf16_t* y1 = ydn; const bf16_t* y2 = ydn; const bf16_t* y3 = ydn; int ny = 0;
.LBB0_1461:
	v_readlane_b32 s4, v255, 0
	v_readlane_b32 s5, v255, 1
	s_and_b64 vcc, exec, s[4:5]
	s_cbranch_vccz .LBB0_1676
	v_readlane_b32 s4, v254, 63
	s_add_i32 s6, s4, 11
	s_load_dword s4, s[0:1], 0xa8
	s_mov_b64 s[14:15], 0
	s_mov_b64 s[40:41], 0
	s_waitcnt lgkmcnt(0)
	s_cmp_ge_i32 s6, s4
	s_cselect_b64 s[4:5], -1, 0
	s_cmp_lt_i32 s6, s69
	s_cselect_b64 s[6:7], -1, 0
	s_and_b64 s[4:5], s[4:5], s[6:7]
	s_and_b64 vcc, exec, s[4:5]
	s_cbranch_vccz .LBB0_1677
	v_mov_b32_e32 v1, v0
	s_mov_b32 s4, s2
	v_ashrrev_i32_e32 v2, 6, v1
	s_nop 0
	v_lshl_add_u32 v48, s4, 3, v2
	v_cmp_gt_i32_e32 vcc, s90, v48
	s_and_saveexec_b64 s[40:41], vcc
	s_cbranch_execz .LBB0_1896
	v_lshlrev_b32_e32 v1, 2, v1
	v_and_b32_e32 v50, 0xfc, v1
	v_lshlrev_b32_e32 v2, 1, v50
	v_and_b32_e32 v1, 64, v227
	v_lshl_add_u64 v[52:53], s[26:27], 0, v[2:3]
	v_add_u32_e32 v1, 64, v1
	v_xor_b32_e32 v2, 32, v227
	v_cmp_lt_i32_e32 vcc, v2, v1
	s_load_dword s4, s[66:67], 0x0
	s_mov_b64 s[42:43], 0
	v_cndmask_b32_e32 v2, v227, v2, vcc
	v_lshlrev_b32_e32 v51, 2, v2
	v_xor_b32_e32 v2, 16, v227
	v_cmp_lt_i32_e32 vcc, v2, v1
	s_waitcnt lgkmcnt(0)
	s_lshl_b32 s44, s4, 3
	s_load_dwordx4 s[4:7], s[0:1], 0x90
	v_cndmask_b32_e32 v2, v227, v2, vcc
	v_lshlrev_b32_e32 v162, 2, v2
	v_xor_b32_e32 v2, 8, v227
	v_cmp_lt_i32_e32 vcc, v2, v1
	s_nop 1
	v_cndmask_b32_e32 v2, v227, v2, vcc
	v_lshlrev_b32_e32 v163, 2, v2
	v_xor_b32_e32 v2, 4, v227
	v_cmp_lt_i32_e32 vcc, v2, v1
	s_nop 1
	v_cndmask_b32_e32 v2, v227, v2, vcc
	v_lshlrev_b32_e32 v164, 2, v2
	v_xor_b32_e32 v2, 2, v227
	v_cmp_lt_i32_e32 vcc, v2, v1
	s_nop 1
	v_cndmask_b32_e32 v2, v227, v2, vcc
	v_lshlrev_b32_e32 v165, 2, v2
	v_xor_b32_e32 v2, 1, v227
	v_cmp_lt_i32_e32 vcc, v2, v1
	s_nop 1
	v_cndmask_b32_e32 v1, v227, v2, vcc
	v_lshlrev_b32_e32 v2, 2, v50
	s_waitcnt lgkmcnt(0)
	v_lshl_add_u64 v[54:55], s[4:5], 0, v[2:3]
	v_readlane_b32 s4, v254, 28
	v_readlane_b32 s5, v254, 29
	v_lshlrev_b32_e32 v166, 2, v1
	v_lshl_add_u64 v[56:57], s[6:7], 0, v[2:3]
	v_lshl_add_u64 v[58:59], s[4:5], 0, v[2:3]
	v_readlane_b32 s4, v254, 30
	v_readlane_b32 s5, v254, 31
	s_nop 1
	v_lshl_add_u64 v[60:61], s[4:5], 0, v[2:3]
	v_readlane_b32 s4, v254, 32
	v_readlane_b32 s5, v254, 33
	s_nop 1
	v_lshl_add_u64 v[62:63], s[4:5], 0, v[2:3]
	v_readlane_b32 s4, v254, 34
	v_readlane_b32 s5, v254, 35
	s_nop 1
	v_lshl_add_u64 v[64:65], s[4:5], 0, v[2:3]
	v_readlane_b32 s4, v254, 22
	v_readlane_b32 s5, v254, 23
	v_and_b32_e32 v249, 15, v0
	v_mul_u32_u24_e32 v249, 0x2400, v249
	v_lshl_add_u32 v249, v48, 2, v249
	v_add_u32_e32 v251, 0x24000, v249
	v_add_u32_e32 v252, 0x48000, v249
	v_add_u32_e32 v167, 0x6c000, v249
	global_load_dword v244, v249, s[4:5]
	global_load_dword v246, v251, s[4:5]
	global_load_dword v247, v252, s[4:5]
	global_load_dword v248, v167, s[4:5]
	s_waitcnt vmcnt(0)
	s_branch .LBB0_1468

; DEVI float bflo(unsigned w) { return __uint_as_float(w << 16); }
; DEVI float bfhi(unsigned w) { return __uint_as_float(w & 0xffff0000u); }
; template <int MODE>
; DEVI void phase_rows(const Params& p, int l, char* smem) {
;     ...
;             {   u32x2 w0[8], w1[8], w2[8], w3[8];
; #pragma unroll
;                 for (int i = 0; i < 8; ++i) { w0[i] = *(const u32x2*)(y0 + i * 256 + lane * 4); w1[i] = *(const u32x2*)(y1 + i * 256 + lane * 4);
;                     w2[i] = *(const u32x2*)(y2 + i * 256 + lane * 4); w3[i] = *(const u32x2*)(y3 + i * 256 + lane * 4); }
;                 const float f0 = ny > 0 ? 1.f : 0.f, f1 = ny > 1 ? 1.f : 0.f, f2 = ny > 2 ? 1.f : 0.f, f3 = ny > 3 ? 1.f : 0.f;
; #pragma unroll
;                 for (int i = 0; i < 8; ++i) {
;                     cacc[i * 4] += f0 * bflo(w0[i][0]) + f1 * bflo(w1[i][0]) + f2 * bflo(w2[i][0]) + f3 * bflo(w3[i][0]);
;                     cacc[i * 4 + 1] += f0 * bfhi(w0[i][0]) + f1 * bfhi(w1[i][0]) + f2 * bfhi(w2[i][0]) + f3 * bfhi(w3[i][0]);
;                     cacc[i * 4 + 2] += f0 * bflo(w0[i][1]) + f1 * bflo(w1[i][1]) + f2 * bflo(w2[i][1]) + f3 * bflo(w3[i][1]);
;                     cacc[i * 4 + 3] += f0 * bfhi(w0[i][1]) + f1 * bfhi(w1[i][1]) + f2 * bfhi(w2[i][1]) + f3 * bfhi(w3[i][1]); }
;             }
;             const float* gf = mrow + 10240;
; #pragma unroll
;             for (int i = 0; i < 8; ++i) { const f32x4 g = *(const f32x4*)(gf + i * 256 + lane * 4);
;                 v[i * 4] += g[0] * cacc[i * 4]; v[i * 4 + 1] += g[1] * cacc[i * 4 + 1]; v[i * 4 + 2] += g[2] * cacc[i * 4 + 2]; v[i * 4 + 3] += g[3] * cacc[i * 4 + 3]; }
.LBB0_1467:
	s_or_b64 exec, exec, s[16:17]
	v_lshlrev_b32_e32 v2, 1, v50
	v_lshl_add_u64 v[96:97], v[78:79], 0, v[2:3]
	v_lshl_add_u64 v[98:99], v[74:75], 0, v[2:3]
	global_load_dwordx2 v[106:107], v[96:97], off
	global_load_dwordx2 v[108:109], v[98:99], off
	global_load_dwordx2 v[120:121], v[96:97], off offset:512
	global_load_dwordx2 v[122:123], v[98:99], off offset:512
	s_waitcnt vmcnt(4)
	v_lshlrev_b32_e32 v104, 16, v46
	v_and_b32_e32 v105, 0xffff0000, v46
	v_lshlrev_b32_e32 v102, 16, v47
	v_and_b32_e32 v103, 0xffff0000, v47
	global_load_dwordx2 v[46:47], v[96:97], off offset:1024
	global_load_dwordx2 v[126:127], v[98:99], off offset:1024
	v_mul_hi_i32_i24_e32 v113, 0xc000, v49
	v_mul_i32_i24_e32 v112, 0xc000, v49
	v_lshlrev_b32_e32 v100, 16, v70
	v_and_b32_e32 v101, 0xffff0000, v70
	v_lshlrev_b32_e32 v110, 16, v71
	v_and_b32_e32 v111, 0xffff0000, v71
	v_lshlrev_b32_e32 v124, 16, v68
	v_and_b32_e32 v125, 0xffff0000, v68
	v_lshlrev_b32_e32 v118, 16, v69
	v_and_b32_e32 v119, 0xffff0000, v69
	v_lshlrev_b32_e32 v94, 16, v44
	v_and_b32_e32 v95, 0xffff0000, v44
	v_lshlrev_b32_e32 v92, 16, v45
	v_and_b32_e32 v93, 0xffff0000, v45
	v_lshlrev_b32_e32 v90, 16, v42
	v_and_b32_e32 v91, 0xffff0000, v42
	global_load_dwordx2 v[44:45], v[96:97], off offset:1536
	global_load_dwordx2 v[128:129], v[98:99], off offset:1536
	v_lshlrev_b32_e32 v88, 16, v43
	v_and_b32_e32 v89, 0xffff0000, v43
	v_lshlrev_b32_e32 v86, 16, v40
	v_and_b32_e32 v87, 0xffff0000, v40
	v_lshlrev_b32_e32 v84, 16, v41
	v_and_b32_e32 v85, 0xffff0000, v41
	v_lshlrev_b32_e32 v82, 16, v38
	v_and_b32_e32 v83, 0xffff0000, v38
	global_load_dwordx2 v[40:41], v[96:97], off offset:2048
	global_load_dwordx2 v[42:43], v[98:99], off offset:2048
	v_lshlrev_b32_e32 v80, 16, v39
	v_and_b32_e32 v81, 0xffff0000, v39
	v_lshlrev_b32_e32 v70, 16, v36
	v_and_b32_e32 v71, 0xffff0000, v36
	v_lshlrev_b32_e32 v68, 16, v37
	v_and_b32_e32 v69, 0xffff0000, v37
	global_load_dwordx2 v[36:37], v[96:97], off offset:2560
	global_load_dwordx2 v[38:39], v[98:99], off offset:2560
	v_cmp_lt_u32_e32 vcc, 2, v116
	v_lshl_add_u64 v[72:73], v[72:73], 0, v[2:3]
	v_lshl_add_u64 v[76:77], v[76:77], 0, v[2:3]
	v_lshl_add_u64 v[134:135], s[82:83], 0, v[112:113]
	v_lshlrev_b32_e32 v2, 2, v50
	v_cndmask_b32_e64 v74, 0, 1.0, vcc
	v_cmp_lt_u32_e32 vcc, 3, v116
	v_lshl_add_u64 v[134:135], v[134:135], 0, v[2:3]
	global_load_dwordx2 v[138:139], v[96:97], off offset:3072
	global_load_dwordx2 v[144:145], v[98:99], off offset:3072
	v_cndmask_b32_e64 v78, 0, 1.0, vcc
	v_add_co_u32_e32 v202, vcc, s62, v134
	global_load_dwordx2 v[180:181], v[96:97], off offset:3584
	global_load_dwordx2 v[182:183], v[98:99], off offset:3584
	global_load_dwordx2 v[184:185], v[72:73], off
	global_load_dwordx2 v[188:189], v[72:73], off offset:512
	global_load_dwordx2 v[190:191], v[72:73], off offset:1024
	global_load_dwordx2 v[150:151], v[72:73], off offset:1536
	global_load_dwordx2 v[186:187], v[76:77], off
	global_load_dwordx2 v[192:193], v[76:77], off offset:512
	global_load_dwordx2 v[194:195], v[76:77], off offset:1024
	global_load_dwordx2 v[152:153], v[76:77], off offset:1536
	global_load_dwordx2 v[130:131], v[72:73], off offset:2048
	global_load_dwordx2 v[112:113], v[72:73], off offset:2560
	global_load_dwordx2 v[96:97], v[72:73], off offset:3072
	s_nop 0
	global_load_dwordx2 v[72:73], v[72:73], off offset:3584
	s_nop 0
	global_load_dwordx2 v[132:133], v[76:77], off offset:2048
	global_load_dwordx2 v[114:115], v[76:77], off offset:2560
	global_load_dwordx2 v[98:99], v[76:77], off offset:3072
	s_nop 0
	global_load_dwordx2 v[76:77], v[76:77], off offset:3584
	v_addc_co_u32_e32 v203, vcc, 0, v135, vcc
	global_load_dwordx4 v[168:171], v[202:203], off offset:-4096
	s_mov_b64 s[4:5], 0xe000
	v_cmp_eq_u32_e32 vcc, 0, v116
	v_add_u32_e32 v48, s44, v48
	s_waitcnt vmcnt(32)
	v_lshlrev_b32_e32 v198, 16, v106
	v_cndmask_b32_e64 v117, 1.0, 0, vcc
	v_cmp_lt_u32_e32 vcc, 1, v116
	s_waitcnt vmcnt(31)
	v_and_b32_e32 v199, 0xffff0000, v108
	v_lshlrev_b32_e32 v200, 16, v108
	v_cndmask_b32_e64 v116, 0, 1.0, vcc
	s_waitcnt vmcnt(28)
	v_lshlrev_b32_e32 v216, 16, v46
	v_and_b32_e32 v219, 0xffff0000, v46
	v_lshlrev_b32_e32 v220, 16, v47
	v_and_b32_e32 v229, 0xffff0000, v47
	v_lshl_add_u64 v[46:47], v[134:135], 0, s[4:5]
	global_load_dwordx4 v[172:175], v[46:47], off offset:1024
	global_load_dwordx4 v[176:179], v[46:47], off offset:2048
	v_and_b32_e32 v201, 0xffff0000, v106
	v_lshlrev_b32_e32 v204, 16, v107
	v_lshlrev_b32_e32 v206, 16, v109
	v_and_b32_e32 v207, 0xffff0000, v107
	v_and_b32_e32 v205, 0xffff0000, v109
	v_lshlrev_b32_e32 v208, 16, v120
	v_lshlrev_b32_e32 v210, 16, v122
	v_and_b32_e32 v211, 0xffff0000, v120
	v_and_b32_e32 v209, 0xffff0000, v122
	v_lshlrev_b32_e32 v212, 16, v121
	v_lshlrev_b32_e32 v214, 16, v123
	v_and_b32_e32 v215, 0xffff0000, v121
	v_and_b32_e32 v213, 0xffff0000, v123
	s_waitcnt vmcnt(28)
	v_lshlrev_b32_e32 v232, 16, v44
	v_and_b32_e32 v237, 0xffff0000, v44
	v_lshlrev_b32_e32 v240, 16, v45
	v_and_b32_e32 v243, 0xffff0000, v45
	v_lshlrev_b32_e32 v228, 16, v127
	v_and_b32_e32 v221, 0xffff0000, v127
	s_waitcnt vmcnt(26)
	v_lshlrev_b32_e32 v158, 16, v40
	s_waitcnt vmcnt(25)
	v_lshlrev_b32_e32 v160, 16, v42
	v_and_b32_e32 v161, 0xffff0000, v40
	v_and_b32_e32 v159, 0xffff0000, v42
	s_waitcnt vmcnt(20)
	v_lshlrev_b32_e32 v120, 16, v180
	s_waitcnt vmcnt(19)
; DEVI float bflo(unsigned w) { return __uint_as_float(w << 16); }
; DEVI float bfhi(unsigned w) { return __uint_as_float(w & 0xffff0000u); }
; template <int MODE>
; DEVI void phase_rows(const Params& p, int l, char* smem) {
;     ...
;                 const float f0 = ny > 0 ? 1.f : 0.f, f1 = ny > 1 ? 1.f : 0.f, f2 = ny > 2 ? 1.f : 0.f, f3 = ny > 3 ? 1.f : 0.f;
; #pragma unroll
;                 for (int i = 0; i < 8; ++i) {
;                     cacc[i * 4] += f0 * bflo(w0[i][0]) + f1 * bflo(w1[i][0]) + f2 * bflo(w2[i][0]) + f3 * bflo(w3[i][0]);
;                     cacc[i * 4 + 1] += f0 * bfhi(w0[i][0]) + f1 * bfhi(w1[i][0]) + f2 * bfhi(w2[i][0]) + f3 * bfhi(w3[i][0]);
;                     cacc[i * 4 + 2] += f0 * bflo(w0[i][1]) + f1 * bflo(w1[i][1]) + f2 * bflo(w2[i][1]) + f3 * bflo(w3[i][1]);
;                     cacc[i * 4 + 3] += f0 * bfhi(w0[i][1]) + f1 * bfhi(w1[i][1]) + f2 * bfhi(w2[i][1]) + f3 * bfhi(w3[i][1]); }
;             }
;             const float* gf = mrow + 10240;
; #pragma unroll
;             for (int i = 0; i < 8; ++i) { const f32x4 g = *(const f32x4*)(gf + i * 256 + lane * 4);
;                 v[i * 4] += g[0] * cacc[i * 4]; v[i * 4 + 1] += g[1] * cacc[i * 4 + 1]; v[i * 4 + 2] += g[2] * cacc[i * 4 + 2]; v[i * 4 + 3] += g[3] * cacc[i * 4 + 3]; }
	v_lshlrev_b32_e32 v122, 16, v182
	v_and_b32_e32 v123, 0xffff0000, v180
	v_lshlrev_b32_e32 v146, 16, v36
	v_and_b32_e32 v149, 0xffff0000, v36
	v_lshlrev_b32_e32 v140, 16, v37
	v_and_b32_e32 v143, 0xffff0000, v37
	v_and_b32_e32 v121, 0xffff0000, v182
	v_lshlrev_b32_e32 v106, 16, v181
	v_lshlrev_b32_e32 v108, 16, v183
	v_and_b32_e32 v109, 0xffff0000, v181
	v_and_b32_e32 v107, 0xffff0000, v183
	global_load_dwordx4 v[180:183], v[46:47], off offset:3072
	v_pk_mul_f32 v[36:37], v[116:117], v[198:199] op_sel:[1,0] op_sel_hi:[0,1]
	v_lshlrev_b32_e32 v148, 16, v38
	v_and_b32_e32 v147, 0xffff0000, v38
	v_lshlrev_b32_e32 v142, 16, v39
	v_and_b32_e32 v141, 0xffff0000, v39
	v_pk_fma_f32 v[36:37], v[116:117], v[200:201], v[36:37]
	s_waitcnt vmcnt(19)
	v_lshlrev_b32_e32 v38, 16, v184
	v_and_b32_e32 v39, 0xffff0000, v184
	v_pk_fma_f32 v[36:37], v[74:75], v[38:39], v[36:37] op_sel_hi:[0,1,1]
	s_waitcnt vmcnt(15)
	v_lshlrev_b32_e32 v38, 16, v186
	v_and_b32_e32 v39, 0xffff0000, v186
	v_pk_fma_f32 v[36:37], v[78:79], v[38:39], v[36:37] op_sel_hi:[0,1,1]
	v_pk_add_f32 v[4:5], v[4:5], v[36:37]
	v_lshlrev_b32_e32 v36, 16, v187
	s_waitcnt vmcnt(3)
	v_pk_fma_f32 v[100:101], v[4:5], v[168:169], v[100:101]
	v_lshlrev_b32_e32 v4, 16, v185
	v_and_b32_e32 v5, 0xffff0000, v185
	v_and_b32_e32 v37, 0xffff0000, v187
	global_load_dwordx4 v[184:187], v[202:203], off
	global_load_dwordx4 v[44:47], v[202:203], off offset:1024
	v_pk_mul_f32 v[38:39], v[116:117], v[204:205] op_sel:[1,0] op_sel_hi:[0,1]
	v_pk_fma_f32 v[38:39], v[116:117], v[206:207], v[38:39]
	v_lshlrev_b32_e32 v154, 16, v41
	v_pk_fma_f32 v[4:5], v[74:75], v[4:5], v[38:39] op_sel_hi:[0,1,1]
	v_lshlrev_b32_e32 v156, 16, v43
	v_and_b32_e32 v157, 0xffff0000, v41
	v_and_b32_e32 v155, 0xffff0000, v43
	v_pk_fma_f32 v[4:5], v[78:79], v[36:37], v[4:5] op_sel_hi:[0,1,1]
	global_load_dwordx4 v[40:43], v[202:203], off offset:2048
	global_load_dwordx4 v[36:39], v[202:203], off offset:3072
	v_lshlrev_b32_e32 v236, 16, v128
	v_and_b32_e32 v233, 0xffff0000, v128
	v_lshlrev_b32_e32 v136, 16, v144
	v_and_b32_e32 v135, 0xffff0000, v144
	v_lshlrev_b32_e32 v128, 16, v145
	v_and_b32_e32 v127, 0xffff0000, v145
	v_pk_mul_f32 v[144:145], v[116:117], v[208:209] op_sel:[1,0] op_sel_hi:[0,1]
	v_pk_fma_f32 v[144:145], v[116:117], v[210:211], v[144:145]
	v_lshlrev_b32_e32 v168, 16, v188
	v_and_b32_e32 v169, 0xffff0000, v188
	v_pk_fma_f32 v[144:145], v[74:75], v[168:169], v[144:145] op_sel_hi:[0,1,1]
	v_lshlrev_b32_e32 v168, 16, v192
	v_and_b32_e32 v169, 0xffff0000, v192
	v_pk_fma_f32 v[168:169], v[78:79], v[168:169], v[144:145] op_sel_hi:[0,1,1]
	v_pk_add_f32 v[8:9], v[8:9], v[168:169]
	v_pk_add_f32 v[4:5], v[6:7], v[4:5]
	s_waitcnt vmcnt(6)
	v_pk_fma_f32 v[8:9], v[8:9], v[172:173], v[124:125]
	v_pk_mul_f32 v[172:173], v[116:117], v[212:213] op_sel:[1,0] op_sel_hi:[0,1]
	v_lshlrev_b32_e32 v168, 16, v189
	v_and_b32_e32 v169, 0xffff0000, v189
	v_pk_fma_f32 v[172:173], v[116:117], v[214:215], v[172:173]
	v_and_b32_e32 v217, 0xffff0000, v126
	v_pk_fma_f32 v[110:111], v[4:5], v[170:171], v[110:111]
	v_lshlrev_b32_e32 v170, 16, v193
	v_and_b32_e32 v171, 0xffff0000, v193
	v_pk_fma_f32 v[168:169], v[74:75], v[168:169], v[172:173] op_sel_hi:[0,1,1]
	v_lshlrev_b32_e32 v218, 16, v126
	v_pk_fma_f32 v[168:169], v[78:79], v[170:171], v[168:169] op_sel_hi:[0,1,1]
	v_pk_mul_f32 v[172:173], v[116:117], v[216:217] op_sel:[1,0] op_sel_hi:[0,1]
	v_pk_add_f32 v[10:11], v[10:11], v[168:169]
	v_lshlrev_b32_e32 v168, 16, v190
	v_and_b32_e32 v169, 0xffff0000, v190
	v_pk_fma_f32 v[172:173], v[116:117], v[218:219], v[172:173]
	v_lshlrev_b32_e32 v170, 16, v194
	v_and_b32_e32 v171, 0xffff0000, v194
	v_pk_fma_f32 v[168:169], v[74:75], v[168:169], v[172:173] op_sel_hi:[0,1,1]
	v_pk_fma_f32 v[168:169], v[78:79], v[170:171], v[168:169] op_sel_hi:[0,1,1]
	v_pk_mul_f32 v[172:173], v[116:117], v[220:221] op_sel:[1,0] op_sel_hi:[0,1]
	v_pk_add_f32 v[12:13], v[12:13], v[168:169]
	v_lshlrev_b32_e32 v168, 16, v191
	v_and_b32_e32 v169, 0xffff0000, v191
	v_pk_fma_f32 v[172:173], v[116:117], v[228:229], v[172:173]
	v_lshlrev_b32_e32 v170, 16, v195
	v_and_b32_e32 v171, 0xffff0000, v195
	v_pk_fma_f32 v[168:169], v[74:75], v[168:169], v[172:173] op_sel_hi:[0,1,1]
	v_pk_fma_f32 v[168:169], v[78:79], v[170:171], v[168:169] op_sel_hi:[0,1,1]
	v_pk_mul_f32 v[172:173], v[116:117], v[232:233] op_sel:[1,0] op_sel_hi:[0,1]
	v_pk_add_f32 v[14:15], v[14:15], v[168:169]
	v_lshlrev_b32_e32 v168, 16, v150
	v_and_b32_e32 v169, 0xffff0000, v150
	v_pk_fma_f32 v[172:173], v[116:117], v[236:237], v[172:173]
	v_lshlrev_b32_e32 v170, 16, v152
	v_and_b32_e32 v171, 0xffff0000, v152
	v_pk_fma_f32 v[168:169], v[74:75], v[168:169], v[172:173] op_sel_hi:[0,1,1]
	v_and_b32_e32 v241, 0xffff0000, v129
	v_pk_fma_f32 v[168:169], v[78:79], v[170:171], v[168:169] op_sel_hi:[0,1,1]
	v_lshlrev_b32_e32 v242, 16, v129
	v_pk_add_f32 v[16:17], v[16:17], v[168:169]
	v_pk_mul_f32 v[168:169], v[116:117], v[240:241] op_sel:[1,0] op_sel_hi:[0,1]
	v_lshlrev_b32_e32 v150, 16, v151
	v_and_b32_e32 v151, 0xffff0000, v151
	v_pk_fma_f32 v[168:169], v[116:117], v[242:243], v[168:169]
	v_lshlrev_b32_e32 v152, 16, v153
	v_and_b32_e32 v153, 0xffff0000, v153
	v_pk_fma_f32 v[150:151], v[74:75], v[150:151], v[168:169] op_sel_hi:[0,1,1]
	v_pk_fma_f32 v[150:151], v[78:79], v[152:153], v[150:151] op_sel_hi:[0,1,1]
	v_pk_add_f32 v[18:19], v[18:19], v[150:151]
	v_pk_mul_f32 v[158:159], v[116:117], v[158:159] op_sel:[1,0] op_sel_hi:[0,1]
	s_waitcnt vmcnt(4)
; DEVI unsigned cvt_pk(float lo, float hi) { f32x2 v = {lo, hi}; bf16x2_t b = __builtin_convertvector(v, bf16x2_t); return __builtin_bit_cast(unsigned, b); }
; DEVI float bflo(unsigned w) { return __uint_as_float(w << 16); }
; DEVI float bfhi(unsigned w) { return __uint_as_float(w & 0xffff0000u); }
; template <int MODE>
; DEVI void phase_rows(const Params& p, int l, char* smem) {
;     ...
;                 for (int i = 0; i < 8; ++i) {
;                     cacc[i * 4] += f0 * bflo(w0[i][0]) + f1 * bflo(w1[i][0]) + f2 * bflo(w2[i][0]) + f3 * bflo(w3[i][0]);
;                     cacc[i * 4 + 1] += f0 * bfhi(w0[i][0]) + f1 * bfhi(w1[i][0]) + f2 * bfhi(w2[i][0]) + f3 * bfhi(w3[i][0]);
;                     cacc[i * 4 + 2] += f0 * bflo(w0[i][1]) + f1 * bflo(w1[i][1]) + f2 * bflo(w2[i][1]) + f3 * bflo(w3[i][1]);
;                     cacc[i * 4 + 3] += f0 * bfhi(w0[i][1]) + f1 * bfhi(w1[i][1]) + f2 * bfhi(w2[i][1]) + f3 * bfhi(w3[i][1]); }
;             }
;             const float* gf = mrow + 10240;
; #pragma unroll
;             for (int i = 0; i < 8; ++i) { const f32x4 g = *(const f32x4*)(gf + i * 256 + lane * 4);
;                 v[i * 4] += g[0] * cacc[i * 4]; v[i * 4 + 1] += g[1] * cacc[i * 4 + 1]; v[i * 4 + 2] += g[2] * cacc[i * 4 + 2]; v[i * 4 + 3] += g[3] * cacc[i * 4 + 3]; }
;             if (MODE == 2) {
; #pragma unroll
;                 for (int i = 0; i < 8; ++i) *(u32x2*)(xres + (size_t)row * DM + i * 256 + lane * 4) = (u32x2){cvt_pk(v[i * 4], v[i * 4 + 1]), cvt_pk(v[i * 4 + 2], v[i * 4 + 3])};
;             }
;         }
;         f32x4 shv[8], scv[8];
;         if (MODE != 3) { const float* mr2 = (MODE == 2) ? mrow + (size_t)5 * 12288 : mrow;
;             const float* sh = mr2 + ((MODE == 1) ? 6144 : 0); const float* sc = mr2 + ((MODE == 1) ? 8192 : 2048);
; #pragma unroll
;             for (int i = 0; i < 8; ++i) { shv[i] = *(const f32x4*)(sh + i * 256 + lane * 4); scv[i] = *(const f32x4*)(sc + i * 256 + lane * 4); } }
;         float ss = 0.f;
; #pragma unroll
;         for (int i = 0; i < 32; ++i) ss += v[i] * v[i];
;         ss = wave_sum(ss);
;         const float rstd = rsqrtf(ss * (1.f / DM) + EPS);
	v_pk_fma_f32 v[92:93], v[18:19], v[182:183], v[92:93]
	v_lshlrev_b32_e32 v18, 16, v130
	v_and_b32_e32 v19, 0xffff0000, v130
	v_pk_fma_f32 v[158:159], v[116:117], v[160:161], v[158:159]
	v_lshlrev_b32_e32 v152, 16, v132
	v_and_b32_e32 v153, 0xffff0000, v132
	v_pk_fma_f32 v[18:19], v[74:75], v[18:19], v[158:159] op_sel_hi:[0,1,1]
	v_pk_fma_f32 v[18:19], v[78:79], v[152:153], v[18:19] op_sel_hi:[0,1,1]
	v_pk_add_f32 v[18:19], v[20:21], v[18:19]
	global_load_dwordx4 v[4:7], v[54:55], off
	global_load_dwordx4 v[198:201], v[54:55], off offset:1024
	global_load_dwordx4 v[202:205], v[54:55], off offset:2048
	global_load_dwordx4 v[206:209], v[54:55], off offset:3072
	global_load_dwordx4 v[210:213], v[58:59], off
	global_load_dwordx4 v[214:217], v[60:61], off
	global_load_dwordx4 v[218:221], v[62:63], off
	global_load_dwordx4 v[168:171], v[64:65], off
	s_waitcnt vmcnt(11)
	v_pk_fma_f32 v[18:19], v[18:19], v[184:185], v[90:91]
	v_lshlrev_b32_e32 v90, 16, v131
	v_and_b32_e32 v91, 0xffff0000, v131
	v_lshlrev_b32_e32 v130, 16, v133
	v_and_b32_e32 v131, 0xffff0000, v133
	v_pk_mul_f32 v[132:133], v[116:117], v[154:155] op_sel:[1,0] op_sel_hi:[0,1]
	v_pk_fma_f32 v[132:133], v[116:117], v[156:157], v[132:133]
	v_lshlrev_b32_e32 v134, 16, v138
	v_and_b32_e32 v137, 0xffff0000, v138
	v_lshlrev_b32_e32 v126, 16, v139
	v_and_b32_e32 v129, 0xffff0000, v139
	v_pk_mul_f32 v[138:139], v[100:101], v[100:101]
	v_pk_fma_f32 v[90:91], v[74:75], v[90:91], v[132:133] op_sel_hi:[0,1,1]
	v_pk_mul_f32 v[144:145], v[110:111], v[110:111]
	v_pk_fma_f32 v[90:91], v[78:79], v[130:131], v[90:91] op_sel_hi:[0,1,1]
	v_pk_mul_f32 v[132:133], v[116:117], v[146:147] op_sel:[1,0] op_sel_hi:[0,1]
	v_add_f32_e32 v1, v138, v139
	v_pk_add_f32 v[22:23], v[22:23], v[90:91]
	v_lshlrev_b32_e32 v90, 16, v112
	v_and_b32_e32 v91, 0xffff0000, v112
	v_pk_fma_f32 v[132:133], v[116:117], v[148:149], v[132:133]
	v_add_f32_e32 v1, v144, v1
	v_pk_mul_f32 v[124:125], v[8:9], v[8:9]
	v_lshlrev_b32_e32 v130, 16, v114
	v_and_b32_e32 v131, 0xffff0000, v114
	v_pk_fma_f32 v[90:91], v[74:75], v[90:91], v[132:133] op_sel_hi:[0,1,1]
	v_add_f32_e32 v1, v145, v1
	v_pk_fma_f32 v[10:11], v[10:11], v[174:175], v[118:119]
	v_pk_fma_f32 v[90:91], v[78:79], v[130:131], v[90:91] op_sel_hi:[0,1,1]
	v_add_f32_e32 v1, v124, v1
	v_pk_mul_f32 v[118:119], v[10:11], v[10:11]
	v_pk_add_f32 v[24:25], v[24:25], v[90:91]
	v_add_f32_e32 v1, v125, v1
	v_pk_fma_f32 v[12:13], v[12:13], v[176:177], v[104:105]
	s_waitcnt vmcnt(10)
	v_pk_fma_f32 v[24:25], v[24:25], v[44:45], v[86:87]
	v_lshlrev_b32_e32 v86, 16, v113
	v_and_b32_e32 v87, 0xffff0000, v113
	v_pk_mul_f32 v[112:113], v[116:117], v[140:141] op_sel:[1,0] op_sel_hi:[0,1]
	v_add_f32_e32 v1, v118, v1
	v_pk_mul_f32 v[104:105], v[12:13], v[12:13]
	v_pk_fma_f32 v[112:113], v[116:117], v[142:143], v[112:113]
	v_add_f32_e32 v1, v119, v1
	v_pk_fma_f32 v[14:15], v[14:15], v[178:179], v[102:103]
	v_lshlrev_b32_e32 v90, 16, v115
	v_and_b32_e32 v91, 0xffff0000, v115
	v_pk_fma_f32 v[86:87], v[74:75], v[86:87], v[112:113] op_sel_hi:[0,1,1]
	v_add_f32_e32 v1, v104, v1
	v_pk_mul_f32 v[102:103], v[14:15], v[14:15]
	v_pk_fma_f32 v[86:87], v[78:79], v[90:91], v[86:87] op_sel_hi:[0,1,1]
	v_add_f32_e32 v1, v105, v1
	v_pk_fma_f32 v[16:17], v[16:17], v[180:181], v[94:95]
	v_pk_add_f32 v[26:27], v[26:27], v[86:87]
	v_pk_mul_f32 v[90:91], v[116:117], v[134:135] op_sel:[1,0] op_sel_hi:[0,1]
	v_add_f32_e32 v1, v102, v1
	v_pk_mul_f32 v[94:95], v[16:17], v[16:17]
	v_pk_fma_f32 v[26:27], v[26:27], v[46:47], v[84:85]
	v_lshlrev_b32_e32 v84, 16, v96
	v_and_b32_e32 v85, 0xffff0000, v96
	v_pk_fma_f32 v[90:91], v[116:117], v[136:137], v[90:91]
	v_add_f32_e32 v1, v103, v1
	v_lshlrev_b32_e32 v86, 16, v98
	v_and_b32_e32 v87, 0xffff0000, v98
	v_pk_fma_f32 v[84:85], v[74:75], v[84:85], v[90:91] op_sel_hi:[0,1,1]
	v_add_f32_e32 v1, v94, v1
	v_pk_mul_f32 v[150:151], v[92:93], v[92:93]
	v_pk_fma_f32 v[84:85], v[78:79], v[86:87], v[84:85] op_sel_hi:[0,1,1]
	v_add_f32_e32 v1, v95, v1
	v_pk_add_f32 v[28:29], v[28:29], v[84:85]
	v_pk_mul_f32 v[86:87], v[116:117], v[126:127] op_sel:[1,0] op_sel_hi:[0,1]
	v_add_f32_e32 v1, v150, v1
	v_pk_mul_f32 v[20:21], v[18:19], v[18:19]
	s_waitcnt vmcnt(9)
	v_pk_fma_f32 v[28:29], v[28:29], v[40:41], v[82:83]
	v_lshlrev_b32_e32 v82, 16, v97
	v_and_b32_e32 v83, 0xffff0000, v97
	v_pk_fma_f32 v[86:87], v[116:117], v[128:129], v[86:87]
	v_add_f32_e32 v1, v151, v1
	v_pk_fma_f32 v[22:23], v[22:23], v[186:187], v[88:89]
	v_lshlrev_b32_e32 v84, 16, v99
	v_and_b32_e32 v85, 0xffff0000, v99
	v_pk_fma_f32 v[82:83], v[74:75], v[82:83], v[86:87] op_sel_hi:[0,1,1]
	v_add_f32_e32 v1, v20, v1
	v_pk_mul_f32 v[88:89], v[22:23], v[22:23]
	v_pk_fma_f32 v[82:83], v[78:79], v[84:85], v[82:83] op_sel_hi:[0,1,1]
	v_add_f32_e32 v1, v21, v1
	v_pk_add_f32 v[30:31], v[30:31], v[82:83]
	v_pk_mul_f32 v[84:85], v[116:117], v[120:121] op_sel:[1,0] op_sel_hi:[0,1]
	v_add_f32_e32 v1, v88, v1
	v_pk_mul_f32 v[44:45], v[24:25], v[24:25]
	v_pk_fma_f32 v[30:31], v[30:31], v[42:43], v[80:81]
	v_lshlrev_b32_e32 v80, 16, v72
	v_and_b32_e32 v81, 0xffff0000, v72
	v_pk_fma_f32 v[84:85], v[116:117], v[122:123], v[84:85]
	v_add_f32_e32 v1, v89, v1
	v_lshlrev_b32_e32 v82, 16, v76
	v_and_b32_e32 v83, 0xffff0000, v76
	v_pk_fma_f32 v[80:81], v[74:75], v[80:81], v[84:85] op_sel_hi:[0,1,1]
	v_add_f32_e32 v1, v44, v1
	v_pk_mul_f32 v[46:47], v[26:27], v[26:27]
	v_pk_fma_f32 v[80:81], v[78:79], v[82:83], v[80:81] op_sel_hi:[0,1,1]
	v_add_f32_e32 v1, v45, v1
	v_pk_add_f32 v[32:33], v[32:33], v[80:81]
	v_add_f32_e32 v1, v46, v1
	v_pk_mul_f32 v[40:41], v[28:29], v[28:29]
	s_waitcnt vmcnt(8)
; template <int MODE>
; DEVI void phase_rows(const Params& p, int l, char* smem) {
;     ...
;         float ss = 0.f;
; #pragma unroll
;         for (int i = 0; i < 32; ++i) ss += v[i] * v[i];
;         ss = wave_sum(ss);
;         const float rstd = rsqrtf(ss * (1.f / DM) + EPS);
;         if (MODE == 3) {
; #pragma unroll
;             for (int i = 0; i < 8; ++i) { const f32x4 g = *(const f32x4*)(p.final_norm + i * 256 + lane * 4);
;                 __builtin_nontemporal_store((f32x4){v[i * 4] * rstd * g[0], v[i * 4 + 1] * rstd * g[1], v[i * 4 + 2] * rstd * g[2], v[i * 4 + 3] * rstd * g[3]}, (f32x4*)(p.out + (size_t)row * DM + i * 256 + lane * 4)); }
;             continue;
	v_pk_fma_f32 v[32:33], v[32:33], v[36:37], v[70:71]
	v_lshlrev_b32_e32 v70, 16, v73
	v_and_b32_e32 v71, 0xffff0000, v73
	v_lshlrev_b32_e32 v72, 16, v77
	v_and_b32_e32 v73, 0xffff0000, v77
	v_pk_mul_f32 v[76:77], v[116:117], v[106:107] op_sel:[1,0] op_sel_hi:[0,1]
	v_add_f32_e32 v1, v47, v1
	v_pk_fma_f32 v[76:77], v[116:117], v[108:109], v[76:77]
	v_add_f32_e32 v1, v40, v1
	v_pk_mul_f32 v[42:43], v[30:31], v[30:31]
	v_pk_fma_f32 v[70:71], v[74:75], v[70:71], v[76:77] op_sel_hi:[0,1,1]
	v_add_f32_e32 v1, v41, v1
	v_pk_fma_f32 v[70:71], v[78:79], v[72:73], v[70:71] op_sel_hi:[0,1,1]
	v_add_f32_e32 v1, v42, v1
	v_pk_mul_f32 v[36:37], v[32:33], v[32:33]
	v_pk_add_f32 v[34:35], v[34:35], v[70:71]
	v_add_f32_e32 v1, v43, v1
	v_pk_fma_f32 v[34:35], v[34:35], v[38:39], v[68:69]
	v_add_f32_e32 v1, v36, v1
	v_pk_mul_f32 v[38:39], v[34:35], v[34:35]
	v_add_f32_e32 v1, v37, v1
	v_add_f32_e32 v1, v38, v1
	v_add_f32_e32 v1, v39, v1
	ds_bpermute_b32 v20, v51, v1
	s_waitcnt lgkmcnt(0)
	v_add_f32_e32 v1, v1, v20
	ds_bpermute_b32 v20, v162, v1
	s_waitcnt lgkmcnt(0)
	v_add_f32_e32 v1, v1, v20
	ds_bpermute_b32 v20, v163, v1
	s_waitcnt lgkmcnt(0)
	v_add_f32_e32 v1, v1, v20
	ds_bpermute_b32 v20, v164, v1
	s_waitcnt lgkmcnt(0)
	v_add_f32_e32 v1, v1, v20
	ds_bpermute_b32 v20, v165, v1
	s_waitcnt lgkmcnt(0)
	v_add_f32_e32 v1, v1, v20
	ds_bpermute_b32 v20, v166, v1
	s_waitcnt lgkmcnt(0)
	v_add_f32_e32 v1, v1, v20
	v_fmamk_f32 v1, v1, 0x3a000000, v223
	v_mul_f32_e32 v20, 0x4b800000, v1
	v_cmp_gt_f32_e32 vcc, s97, v1
	s_nop 1
	v_cndmask_b32_e32 v1, v1, v20, vcc
	v_rsq_f32_e32 v1, v1
	v_lshlrev_b64 v[20:21], 2, v[66:67]
	v_lshl_add_u64 v[36:37], v[56:57], 0, v[20:21]
	v_mul_f32_e32 v38, 0x45800000, v1
	v_cndmask_b32_e32 v38, v1, v38, vcc
	v_pk_mul_f32 v[40:41], v[100:101], v[38:39] op_sel_hi:[1,0]
	v_pk_mul_f32 v[42:43], v[110:111], v[38:39] op_sel_hi:[1,0]
	s_waitcnt vmcnt(0)
	v_pk_mul_f32 v[4:5], v[4:5], v[40:41]
	v_pk_mul_f32 v[6:7], v[6:7], v[42:43]
	global_store_dwordx4 v[36:37], v[4:7], off nt
	s_load_dwordx4 s[4:7], s[0:1], 0x90
	v_pk_mul_f32 v[10:11], v[10:11], v[38:39] op_sel_hi:[1,0]
	v_pk_mul_f32 v[8:9], v[8:9], v[38:39] op_sel_hi:[1,0]
	s_waitcnt lgkmcnt(0)
	s_movk_i32 s4, 0x1000
	v_lshl_add_u64 v[20:21], s[6:7], 0, v[20:21]
	v_lshl_add_u64 v[20:21], v[20:21], 0, v[2:3]
	v_pk_mul_f32 v[4:5], v[198:199], v[8:9]
	v_pk_mul_f32 v[6:7], v[200:201], v[10:11]
	global_store_dwordx4 v[20:21], v[4:7], off offset:1024 nt
	v_pk_mul_f32 v[8:9], v[14:15], v[38:39] op_sel_hi:[1,0]
	v_pk_mul_f32 v[10:11], v[12:13], v[38:39] op_sel_hi:[1,0]
	v_pk_mul_f32 v[12:13], v[18:19], v[38:39] op_sel_hi:[1,0]
	v_pk_mul_f32 v[4:5], v[202:203], v[10:11]
	v_pk_mul_f32 v[6:7], v[204:205], v[8:9]
	global_store_dwordx4 v[20:21], v[4:7], off offset:2048 nt
	v_pk_mul_f32 v[8:9], v[92:93], v[38:39] op_sel_hi:[1,0]
	v_pk_mul_f32 v[10:11], v[16:17], v[38:39] op_sel_hi:[1,0]
	v_pk_mul_f32 v[6:7], v[208:209], v[8:9]
	v_pk_mul_f32 v[4:5], v[206:207], v[10:11]
	global_store_dwordx4 v[20:21], v[4:7], off offset:3072 nt
	v_add_co_u32_e32 v8, vcc, s4, v20
	v_pk_mul_f32 v[10:11], v[22:23], v[38:39] op_sel_hi:[1,0]
	s_nop 0
	v_addc_co_u32_e32 v9, vcc, 0, v21, vcc
	v_cmp_lt_i32_e32 vcc, s73, v48
	s_or_b64 s[42:43], vcc, s[42:43]
	v_pk_mul_f32 v[4:5], v[210:211], v[12:13]
	v_pk_mul_f32 v[6:7], v[212:213], v[10:11]
	global_store_dwordx4 v[8:9], v[4:7], off nt
	v_pk_mul_f32 v[10:11], v[26:27], v[38:39] op_sel_hi:[1,0]
	v_pk_mul_f32 v[12:13], v[24:25], v[38:39] op_sel_hi:[1,0]
	v_pk_mul_f32 v[6:7], v[216:217], v[10:11]
	v_pk_mul_f32 v[4:5], v[214:215], v[12:13]
	global_store_dwordx4 v[8:9], v[4:7], off offset:1024 nt
	v_pk_mul_f32 v[10:11], v[30:31], v[38:39] op_sel_hi:[1,0]
	v_pk_mul_f32 v[12:13], v[28:29], v[38:39] op_sel_hi:[1,0]
	v_pk_mul_f32 v[6:7], v[220:221], v[10:11]
	v_pk_mul_f32 v[4:5], v[218:219], v[12:13]
	global_store_dwordx4 v[8:9], v[4:7], off offset:2048 nt
	v_pk_mul_f32 v[10:11], v[34:35], v[38:39] op_sel_hi:[1,0]
	v_pk_mul_f32 v[12:13], v[32:33], v[38:39] op_sel_hi:[1,0]
	v_pk_mul_f32 v[6:7], v[170:171], v[10:11]
	v_pk_mul_f32 v[4:5], v[168:169], v[12:13]
	global_store_dwordx4 v[8:9], v[4:7], off offset:3072 nt
	s_andn2_b64 exec, exec, s[42:43]
	s_cbranch_execz .LBB0_1896
; DEVI float bflo(unsigned w) { return __uint_as_float(w << 16); }
; DEVI float bfhi(unsigned w) { return __uint_as_float(w & 0xffff0000u); }
; DEVI int obid() { int b = blockIdx.x; asm volatile("" : "+s"(b)); return b; }
; template <int MODE>
; DEVI void phase_rows(const Params& p, int l, char* smem) {
;     ...
;     for (int row = obid() * 8 + wid; row < nrows; row += gridDim.x * 8) {
;         const bool lat = row < NLAT;
;         const int b = lat ? (row >> 11) : ((row - NLAT) >> 8);
;         const int tok = lat ? (row & 2047) : (SEQ + ((row - NLAT) & 255));
;         float v[32];
;         if (MODE == 0) { const float* src = lat ? p.x + (size_t)row * DM : p.ctx + (size_t)(row - NLAT) * DM;
; #pragma unroll
;             for (int i = 0; i < 8; ++i) { const f32x4 t = *(const f32x4*)(src + i * 256 + lane * 4); v[i * 4] = t[0]; v[i * 4 + 1] = t[1]; v[i * 4 + 2] = t[2]; v[i * 4 + 3] = t[3]; }
;         } else { const bf16_t* src = xres + (size_t)row * DM;
; #pragma unroll
;             for (int i = 0; i < 8; ++i) { const u32x2 t = *(const u32x2*)(src + i * 256 + lane * 4); v[i * 4] = bflo(t[0]); v[i * 4 + 1] = bfhi(t[0]); v[i * 4 + 2] = bflo(t[1]); v[i * 4 + 3] = bfhi(t[1]); }
;         }
;         const float* mrow = mod + (size_t)(((MODE == 2) ? l : l) * 5 + (lat ? b : 4)) * 12288;
;         if (MODE == 2 || MODE == 3) {
;             float cacc[32];
; #pragma unroll
;             for (int i = 0; i < 32; ++i) cacc[i] = 0.f;
;             const int* rk = (const int*)(p.ws + WS_RANK) + (size_t)b * 16 * KEYS + tok;
;             const bf16_t* ydn = (const bf16_t*)(p.ws + WS_YDN);
;             const int cap = lat ? 256 : 32;
;             int rke[16];
; #pragma unroll
;             for (int e = 0; e < 16; ++e) rke[e] = rk[e * KEYS];
;             const bf16_t* y0 = ydn; const bf16_t* y1 = ydn; const bf16_t* y2 = ydn; const bf16_t* y3 = ydn; int ny = 0;
; #pragma unroll
;             for (int e = 0; e < 16; ++e) {
;                 const int r = rke[e];
;                 if (r < cap) {
;                     const int slot = lat ? (b * 256 + r) : (1024 + b * 32 + r);
;                     const bf16_t* yr = ydn + ((size_t)e * MSLOT + slot) * DM;
;                     if (ny == 0) y0 = yr; else if (ny == 1) y1 = yr; else if (ny == 2) y2 = yr; else if (ny == 3) y3 = yr;
.LBB0_1468:
	v_ashrrev_i32_e32 v49, 31, v48
	s_nop 0
	v_lshlrev_b64 v[4:5], 12, v[48:49]
	v_ashrrev_i32_e32 v6, 11, v48
	v_lshl_add_u64 v[4:5], v[52:53], 0, v[4:5]
	v_readlane_b32 s4, v254, 22
	global_load_dwordx2 v[70:71], v[4:5], off
	global_load_dwordx2 v[68:69], v[4:5], off offset:512
	global_load_dwordx2 v[46:47], v[4:5], off offset:1024
	global_load_dwordx2 v[44:45], v[4:5], off offset:1536
	global_load_dwordx2 v[42:43], v[4:5], off offset:2048
	global_load_dwordx2 v[40:41], v[4:5], off offset:2560
	global_load_dwordx2 v[38:39], v[4:5], off offset:3072
	global_load_dwordx2 v[36:37], v[4:5], off offset:3584
	v_and_b32_e32 v1, 0x7ff, v48
	v_mul_hi_i32_i24_e32 v5, 0x24000, v6
	v_mul_i32_i24_e32 v4, 0x24000, v6
	v_readlane_b32 s5, v254, 23
	v_lshlrev_b32_e32 v2, 2, v1
	v_lshlrev_b32_e32 v85, 8, v6
	v_lshl_add_u64 v[4:5], s[4:5], 0, v[4:5]
	v_lshl_add_u64 v[8:9], v[4:5], 0, v[2:3]
	v_add_co_u32_e32 v4, vcc, s90, v8
	s_movk_i32 s4, 0x4000
	s_nop 0
	v_addc_co_u32_e32 v5, vcc, 0, v9, vcc
	v_add_co_u32_e32 v10, vcc, s4, v8
	s_movk_i32 s4, 0x6000
	s_nop 0
	v_addc_co_u32_e32 v11, vcc, 0, v9, vcc
	v_mov_b32_e32 v249, 0
	ds_bpermute_b32 v7, v249, v244
	v_mov_b64_e32 v[74:75], s[70:71]
	v_mov_b32_e32 v251, 4
	ds_bpermute_b32 v5, v251, v244
	s_waitcnt lgkmcnt(0)
	v_cmp_gt_i32_e64 s[38:39], s92, v5
	v_mov_b32_e32 v252, 8
	ds_bpermute_b32 v4, v252, v244
	v_add_co_u32_e32 v10, vcc, s4, v8
	s_mov_b32 s4, 0x9000
	s_nop 0
	v_addc_co_u32_e32 v11, vcc, 0, v9, vcc
	v_mov_b32_e32 v167, 12
	ds_bpermute_b32 v2, v167, v244
	v_add_co_u32_e32 v10, vcc, s4, v8
	s_mov_b32 s4, 0xb000
	s_nop 0
	v_addc_co_u32_e32 v11, vcc, 0, v9, vcc
	v_mov_b32_e32 v249, 16
	ds_bpermute_b32 v80, v249, v244
	v_add_co_u32_e32 v10, vcc, s4, v8
	s_mov_b32 s4, 0xd000
	s_nop 0
	v_addc_co_u32_e32 v11, vcc, 0, v9, vcc
	v_mov_b32_e32 v251, 20
	ds_bpermute_b32 v94, v251, v244
	v_add_co_u32_e32 v10, vcc, s4, v8
	s_mov_b32 s4, 0x12000
	s_nop 0
	v_addc_co_u32_e32 v11, vcc, 0, v9, vcc
	v_mov_b32_e32 v252, 24
	ds_bpermute_b32 v93, v252, v244
	v_add_co_u32_e32 v10, vcc, s62, v8
	s_nop 1
	v_addc_co_u32_e32 v11, vcc, 0, v9, vcc
	v_mov_b32_e32 v167, 28
	ds_bpermute_b32 v92, v167, v244
	v_add_co_u32_e32 v10, vcc, s4, v8
	s_mov_b32 s4, 0x14000
	s_nop 0
	v_addc_co_u32_e32 v11, vcc, 0, v9, vcc
	v_mov_b32_e32 v249, 32
	ds_bpermute_b32 v1, v249, v244
	v_add_co_u32_e32 v10, vcc, s4, v8
	s_mov_b32 s4, 0x16000
	s_nop 0
	v_addc_co_u32_e32 v11, vcc, 0, v9, vcc
	v_mov_b32_e32 v251, 36
	ds_bpermute_b32 v91, v251, v244
	v_add_co_u32_e32 v10, vcc, s4, v8
	s_mov_b32 s4, 0x18000
	s_nop 0
	v_addc_co_u32_e32 v11, vcc, 0, v9, vcc
	v_mov_b32_e32 v252, 40
	ds_bpermute_b32 v90, v252, v244
	v_add_co_u32_e32 v10, vcc, s4, v8
	s_mov_b32 s4, 0x1b000
	s_nop 0
	v_addc_co_u32_e32 v11, vcc, 0, v9, vcc
	v_mov_b32_e32 v167, 44
	ds_bpermute_b32 v89, v167, v244
	v_add_co_u32_e32 v10, vcc, s4, v8
	s_mov_b32 s4, 0x1d000
	s_nop 0
	v_addc_co_u32_e32 v11, vcc, 0, v9, vcc
	v_mov_b32_e32 v249, 48
	ds_bpermute_b32 v88, v249, v244
	v_add_co_u32_e32 v10, vcc, s4, v8
	s_mov_b32 s4, 0x1f000
	s_nop 0
	v_addc_co_u32_e32 v11, vcc, 0, v9, vcc
	v_mov_b32_e32 v251, 52
	ds_bpermute_b32 v87, v251, v244
	v_add_co_u32_e32 v10, vcc, s4, v8
	s_mov_b32 s4, 0x21000
	s_nop 0
	v_addc_co_u32_e32 v11, vcc, 0, v9, vcc
	v_add_co_u32_e32 v8, vcc, s4, v8
	v_mov_b32_e32 v252, 56
	ds_bpermute_b32 v86, v252, v244
	s_nop 0
	v_addc_co_u32_e32 v9, vcc, 0, v9, vcc
	v_mov_b32_e32 v167, 60
	ds_bpermute_b32 v84, v167, v244
	v_add_u32_e32 v8, v7, v85
	v_ashrrev_i32_e32 v9, 31, v8
	v_cmp_gt_i32_e32 vcc, s92, v7
	v_lshlrev_b64 v[8:9], 12, v[8:9]
	s_nop 0
	v_cndmask_b32_e32 v9, 0, v9, vcc
	v_cndmask_b32_e32 v8, 0, v8, vcc
	v_cndmask_b32_e64 v116, 0, 1, vcc
	v_lshl_add_u64 v[78:79], s[70:71], 0, v[8:9]
	s_and_saveexec_b64 s[16:17], s[38:39]
	s_cbranch_execz .LBB0_1470
	v_add_u32_e32 v8, v5, v85
	v_ashrrev_i32_e32 v9, 31, v8
	v_lshlrev_b64 v[8:9], 12, v[8:9]
	v_lshl_add_u64 v[8:9], s[70:71], 0, v[8:9]
	s_mov_b64 s[4:5], 0x500000
	v_lshl_add_u64 v[8:9], v[8:9], 0, s[4:5]
	v_mov_b32_e32 v5, s71
	v_cndmask_b32_e32 v75, v5, v9, vcc
	v_mov_b32_e32 v5, s70
	v_cndmask_b32_e32 v74, v5, v8, vcc
	v_cndmask_b32_e32 v79, v9, v79, vcc
	v_cndmask_b32_e32 v78, v8, v78, vcc
	v_cndmask_b32_e64 v116, 1, 2, vcc
.LBB0_1470:
	s_or_b64 exec, exec, s[16:17]
	s_waitcnt lgkmcnt(0)
	v_mov_b32_e32 v244, v246
	v_mov_b32_e32 v246, v247
	v_mov_b32_e32 v247, v248
	v_cmp_gt_i32_e32 vcc, s92, v4
	v_mov_b64_e32 v[72:73], s[70:71]
	s_and_saveexec_b64 s[16:17], vcc
	s_cbranch_execz .LBB0_1476
	v_cmp_lt_i32_e32 vcc, 1, v116
	s_and_saveexec_b64 s[4:5], vcc
	s_xor_b64 s[28:29], exec, s[4:5]
	s_or_saveexec_b64 s[28:29], s[28:29]
	v_add_u32_e32 v4, v4, v85
	v_ashrrev_i32_e32 v5, 31, v4
	v_lshlrev_b64 v[4:5], 12, v[4:5]
	v_lshl_add_u64 v[4:5], s[70:71], 0, v[4:5]
	s_mov_b64 s[4:5], 0xa00000
	v_lshl_add_u64 v[72:73], v[4:5], 0, s[4:5]
	s_xor_b64 exec, exec, s[28:29]
	s_cbranch_execz .LBB0_1475
	v_cmp_eq_u32_e32 vcc, 1, v116
	v_mov_b64_e32 v[4:5], v[72:73]
	s_and_saveexec_b64 s[34:35], vcc
	v_mov_b64_e32 v[4:5], v[78:79]
	v_mov_b64_e32 v[74:75], v[72:73]
	s_or_b64 exec, exec, s[34:35]
	v_mov_b64_e32 v[72:73], s[70:71]
	v_mov_b64_e32 v[78:79], v[4:5]

; DEVI float bflo(unsigned w) { return __uint_as_float(w << 16); }
; DEVI float bfhi(unsigned w) { return __uint_as_float(w & 0xffff0000u); }
; template <int MODE>
; DEVI void phase_rows(const Params& p, int l, char* smem) {
;     ...
;             for (int e = 0; e < 16; ++e) {
;                 const int r = rke[e];
;                 if (r < cap) {
;                     const int slot = lat ? (b * 256 + r) : (1024 + b * 32 + r);
;                     const bf16_t* yr = ydn + ((size_t)e * MSLOT + slot) * DM;
;                     if (ny == 0) y0 = yr; else if (ny == 1) y1 = yr; else if (ny == 2) y2 = yr; else if (ny == 3) y3 = yr;
;                     else {
; #pragma unroll
;                         for (int i = 0; i < 8; ++i) { const u32x2 w = *(const u32x2*)(yr + i * 256 + lane * 4);
;                             cacc[i * 4] += bflo(w[0]); cacc[i * 4 + 1] += bfhi(w[0]); cacc[i * 4 + 2] += bflo(w[1]); cacc[i * 4 + 3] += bfhi(w[1]); }
;                     }
;                     ++ny;
.LBB0_1476:
	s_or_b64 exec, exec, s[16:17]
	v_lshlrev_b64 v[66:67], 11, v[48:49]
	v_add_u32_e32 v49, 5, v6
	v_cmp_gt_i32_e32 vcc, s92, v2
	v_mov_b64_e32 v[76:77], s[70:71]
	s_and_saveexec_b64 s[16:17], vcc
	s_cbranch_execz .LBB0_1486
	v_add_u32_e32 v4, v2, v85
	v_ashrrev_i32_e32 v5, 31, v4
	v_lshlrev_b64 v[4:5], 12, v[4:5]
	v_lshl_add_u64 v[4:5], s[70:71], 0, v[4:5]
	s_mov_b64 s[4:5], 0xf00000
	v_lshl_add_u64 v[76:77], v[4:5], 0, s[4:5]
	v_cmp_lt_i32_e32 vcc, 1, v116
	s_and_saveexec_b64 s[4:5], vcc
	s_xor_b64 s[28:29], exec, s[4:5]
	s_cbranch_execz .LBB0_1481
	v_cmp_lt_i32_e32 vcc, 2, v116
	s_and_saveexec_b64 s[4:5], vcc
	s_xor_b64 s[34:35], exec, s[4:5]
	s_andn2_saveexec_b64 s[34:35], s[34:35]
	v_mov_b64_e32 v[72:73], v[76:77]
	v_mov_b64_e32 v[76:77], s[70:71]
	s_or_b64 exec, exec, s[34:35]

; DEVI float bflo(unsigned w) { return __uint_as_float(w << 16); }
; DEVI float bfhi(unsigned w) { return __uint_as_float(w & 0xffff0000u); }
; template <int MODE>
; DEVI void phase_rows(const Params& p, int l, char* smem) {
;     ...
;             for (int i = 0; i < 32; ++i) cacc[i] = 0.f;
;             const int* rk = (const int*)(p.ws + WS_RANK) + (size_t)b * 16 * KEYS + tok;
;             const bf16_t* ydn = (const bf16_t*)(p.ws + WS_YDN);
;             const int cap = lat ? 256 : 32;
;             int rke[16];
; #pragma unroll
;             for (int e = 0; e < 16; ++e) rke[e] = rk[e * KEYS];
;             const bf16_t* y0 = ydn; const bf16_t* y1 = ydn; const bf16_t* y2 = ydn; const bf16_t* y3 = ydn; int ny = 0;
; #pragma unroll
;             for (int e = 0; e < 16; ++e) {
;                 const int r = rke[e];
;                 if (r < cap) {
;                     const int slot = lat ? (b * 256 + r) : (1024 + b * 32 + r);
;                     const bf16_t* yr = ydn + ((size_t)e * MSLOT + slot) * DM;
;                     if (ny == 0) y0 = yr; else if (ny == 1) y1 = yr; else if (ny == 2) y2 = yr; else if (ny == 3) y3 = yr;
;                     else {
; #pragma unroll
;                         for (int i = 0; i < 8; ++i) { const u32x2 w = *(const u32x2*)(yr + i * 256 + lane * 4);
;                             cacc[i * 4] += bflo(w[0]); cacc[i * 4 + 1] += bfhi(w[0]); cacc[i * 4 + 2] += bflo(w[1]); cacc[i * 4 + 3] += bfhi(w[1]); }
;                     }
;                     ++ny;
.LBB0_1486:
	s_or_b64 exec, exec, s[16:17]
	v_mov_b32_e32 v4, v3
	v_mov_b32_e32 v5, v3
	v_mov_b32_e32 v6, v3
	v_mov_b32_e32 v7, v3
	v_mov_b32_e32 v8, v3
	v_mov_b32_e32 v9, v3
	v_mov_b32_e32 v10, v3
	v_mov_b32_e32 v11, v3
	v_mov_b32_e32 v12, v3
	v_mov_b32_e32 v13, v3
	v_mov_b32_e32 v14, v3
	v_mov_b32_e32 v15, v3
	v_mov_b32_e32 v16, v3
	v_mov_b32_e32 v17, v3
	v_mov_b32_e32 v18, v3
	v_mov_b32_e32 v19, v3
	v_mov_b32_e32 v20, v3
	v_mov_b32_e32 v21, v3
	v_mov_b32_e32 v22, v3
	v_mov_b32_e32 v23, v3
	v_mov_b32_e32 v24, v3
	v_mov_b32_e32 v25, v3
	v_mov_b32_e32 v26, v3
	v_mov_b32_e32 v27, v3
	v_mov_b32_e32 v28, v3
	v_mov_b32_e32 v29, v3
	v_mov_b32_e32 v30, v3
	v_mov_b32_e32 v31, v3
	v_mov_b32_e32 v32, v3
	v_mov_b32_e32 v33, v3
	v_mov_b32_e32 v2, v3
	v_mov_b64_e32 v[34:35], v[32:33]
	v_cmp_gt_i32_e32 vcc, s92, v80
	v_mov_b64_e32 v[32:33], v[30:31]
	v_mov_b64_e32 v[30:31], v[28:29]
	v_mov_b64_e32 v[28:29], v[26:27]
	v_mov_b64_e32 v[26:27], v[24:25]
	v_mov_b64_e32 v[24:25], v[22:23]
	v_mov_b64_e32 v[22:23], v[20:21]
	v_mov_b64_e32 v[20:21], v[18:19]
	v_mov_b64_e32 v[18:19], v[16:17]
	v_mov_b64_e32 v[16:17], v[14:15]
	v_mov_b64_e32 v[14:15], v[12:13]
	v_mov_b64_e32 v[12:13], v[10:11]
	v_mov_b64_e32 v[10:11], v[8:9]
	v_mov_b64_e32 v[8:9], v[6:7]
	v_mov_b64_e32 v[6:7], v[4:5]
	v_mov_b64_e32 v[4:5], v[2:3]
	s_and_saveexec_b64 s[16:17], vcc
	s_cbranch_execz .LBB0_1582
	v_add_u32_e32 v4, v80, v85
	v_ashrrev_i32_e32 v5, 31, v4
	v_lshlrev_b64 v[4:5], 12, v[4:5]
	v_lshl_add_u64 v[4:5], s[70:71], 0, v[4:5]
	s_mov_b64 s[4:5], 0x1400000
	v_lshl_add_u64 v[80:81], v[4:5], 0, s[4:5]
	v_cmp_lt_i32_e32 vcc, 1, v116
	s_and_saveexec_b64 s[4:5], vcc
	s_xor_b64 s[38:39], exec, s[4:5]
	s_cbranch_execz .LBB0_1497
	v_cmp_lt_i32_e32 vcc, 2, v116
	s_and_saveexec_b64 s[4:5], vcc
	s_xor_b64 s[28:29], exec, s[4:5]
	s_cbranch_execz .LBB0_1494
	v_cmp_ne_u32_e32 vcc, 3, v116
	s_and_saveexec_b64 s[4:5], vcc
	s_xor_b64 s[34:35], exec, s[4:5]
	s_cbranch_execz .LBB0_1491
	v_lshlrev_b32_e32 v2, 1, v50
	v_lshl_add_u64 v[32:33], v[80:81], 0, v[2:3]
	global_load_dwordx2 v[6:7], v[32:33], off
	global_load_dwordx2 v[10:11], v[32:33], off offset:512
	global_load_dwordx2 v[14:15], v[32:33], off offset:1024
	global_load_dwordx2 v[18:19], v[32:33], off offset:1536
	global_load_dwordx2 v[22:23], v[32:33], off offset:2048
	global_load_dwordx2 v[26:27], v[32:33], off offset:2560
	global_load_dwordx2 v[30:31], v[32:33], off offset:3072
	global_load_dwordx2 v[34:35], v[32:33], off offset:3584
	s_waitcnt vmcnt(7)
	v_lshlrev_b32_e32 v4, 16, v6
	v_and_b32_e32 v5, 0xffff0000, v6
	v_lshlrev_b32_e32 v6, 16, v7
	v_and_b32_e32 v7, 0xffff0000, v7
	s_waitcnt vmcnt(6)
	v_lshlrev_b32_e32 v8, 16, v10
	v_and_b32_e32 v9, 0xffff0000, v10
	v_lshlrev_b32_e32 v10, 16, v11
	v_and_b32_e32 v11, 0xffff0000, v11
	s_waitcnt vmcnt(5)
	v_lshlrev_b32_e32 v12, 16, v14
	v_and_b32_e32 v13, 0xffff0000, v14
	v_lshlrev_b32_e32 v14, 16, v15
	v_and_b32_e32 v15, 0xffff0000, v15
	s_waitcnt vmcnt(4)
	v_lshlrev_b32_e32 v16, 16, v18
	v_and_b32_e32 v17, 0xffff0000, v18
	v_lshlrev_b32_e32 v18, 16, v19
	v_and_b32_e32 v19, 0xffff0000, v19
	s_waitcnt vmcnt(3)
	v_lshlrev_b32_e32 v20, 16, v22
	v_and_b32_e32 v21, 0xffff0000, v22
	v_lshlrev_b32_e32 v22, 16, v23
	v_and_b32_e32 v23, 0xffff0000, v23
	s_waitcnt vmcnt(2)
	v_lshlrev_b32_e32 v24, 16, v26
	v_and_b32_e32 v25, 0xffff0000, v26
	v_lshlrev_b32_e32 v26, 16, v27
	v_and_b32_e32 v27, 0xffff0000, v27
	s_waitcnt vmcnt(1)
	v_lshlrev_b32_e32 v28, 16, v30
	v_and_b32_e32 v29, 0xffff0000, v30
	v_lshlrev_b32_e32 v30, 16, v31
	v_and_b32_e32 v31, 0xffff0000, v31
	s_waitcnt vmcnt(0)
	v_lshlrev_b32_e32 v32, 16, v34
	v_and_b32_e32 v33, 0xffff0000, v34
	v_lshlrev_b32_e32 v34, 16, v35
	v_and_b32_e32 v35, 0xffff0000, v35
	v_pk_add_f32 v[4:5], v[4:5], 0 op_sel_hi:[1,0]
	v_pk_add_f32 v[6:7], v[6:7], 0 op_sel_hi:[1,0]
	v_pk_add_f32 v[8:9], v[8:9], 0 op_sel_hi:[1,0]
	v_pk_add_f32 v[10:11], v[10:11], 0 op_sel_hi:[1,0]
	v_pk_add_f32 v[12:13], v[12:13], 0 op_sel_hi:[1,0]
	v_pk_add_f32 v[14:15], v[14:15], 0 op_sel_hi:[1,0]
	v_pk_add_f32 v[16:17], v[16:17], 0 op_sel_hi:[1,0]
	v_pk_add_f32 v[18:19], v[18:19], 0 op_sel_hi:[1,0]
	v_pk_add_f32 v[20:21], v[20:21], 0 op_sel_hi:[1,0]
	v_pk_add_f32 v[22:23], v[22:23], 0 op_sel_hi:[1,0]
	v_pk_add_f32 v[24:25], v[24:25], 0 op_sel_hi:[1,0]
	v_pk_add_f32 v[26:27], v[26:27], 0 op_sel_hi:[1,0]
	v_pk_add_f32 v[28:29], v[28:29], 0 op_sel_hi:[1,0]
	v_pk_add_f32 v[30:31], v[30:31], 0 op_sel_hi:[1,0]
	v_pk_add_f32 v[32:33], v[32:33], 0 op_sel_hi:[1,0]
	v_pk_add_f32 v[34:35], v[34:35], 0 op_sel_hi:[1,0]

; DEVI float bflo(unsigned w) { return __uint_as_float(w << 16); }
; DEVI float bfhi(unsigned w) { return __uint_as_float(w & 0xffff0000u); }
; template <int MODE>
; DEVI void phase_rows(const Params& p, int l, char* smem) {
;     ...
;             for (int e = 0; e < 16; ++e) {
;                 const int r = rke[e];
;                 if (r < cap) {
;                     const int slot = lat ? (b * 256 + r) : (1024 + b * 32 + r);
;                     const bf16_t* yr = ydn + ((size_t)e * MSLOT + slot) * DM;
;                     if (ny == 0) y0 = yr; else if (ny == 1) y1 = yr; else if (ny == 2) y2 = yr; else if (ny == 3) y3 = yr;
;                     else {
; #pragma unroll
;                         for (int i = 0; i < 8; ++i) { const u32x2 w = *(const u32x2*)(yr + i * 256 + lane * 4);
;                             cacc[i * 4] += bflo(w[0]); cacc[i * 4 + 1] += bfhi(w[0]); cacc[i * 4 + 2] += bflo(w[1]); cacc[i * 4 + 3] += bfhi(w[1]); }
;                     }
;                     ++ny;
;                 }
;             }
.LBB0_1501:
	s_or_b64 exec, exec, s[28:29]
	v_add_u32_e32 v116, 1, v116
	s_or_b64 exec, exec, s[16:17]
	v_cmp_gt_i32_e32 vcc, s92, v94
	s_and_saveexec_b64 s[16:17], vcc
	s_cbranch_execnz .LBB0_1583
.LBB0_1502:
	s_or_b64 exec, exec, s[16:17]
	v_cmp_gt_i32_e32 vcc, s92, v93
	s_and_saveexec_b64 s[16:17], vcc
	s_cbranch_execz .LBB0_1598

; DEVI float bflo(unsigned w) { return __uint_as_float(w << 16); }
; DEVI float bfhi(unsigned w) { return __uint_as_float(w & 0xffff0000u); }
; template <int MODE>
; DEVI void phase_rows(const Params& p, int l, char* smem) {
;     ...
;             for (int e = 0; e < 16; ++e) {
;                 const int r = rke[e];
;                 if (r < cap) {
;                     const int slot = lat ? (b * 256 + r) : (1024 + b * 32 + r);
;                     const bf16_t* yr = ydn + ((size_t)e * MSLOT + slot) * DM;
;                     if (ny == 0) y0 = yr; else if (ny == 1) y1 = yr; else if (ny == 2) y2 = yr; else if (ny == 3) y3 = yr;
;                     else {
; #pragma unroll
;                         for (int i = 0; i < 8; ++i) { const u32x2 w = *(const u32x2*)(yr + i * 256 + lane * 4);
;                             cacc[i * 4] += bflo(w[0]); cacc[i * 4 + 1] += bfhi(w[0]); cacc[i * 4 + 2] += bflo(w[1]); cacc[i * 4 + 3] += bfhi(w[1]); }
;                     }
;                     ++ny;
;                 }
;             }
.LBB0_1517:
	s_or_b64 exec, exec, s[28:29]
	v_add_u32_e32 v116, 1, v116
	s_or_b64 exec, exec, s[16:17]
	v_cmp_gt_i32_e32 vcc, s92, v92
	s_and_saveexec_b64 s[16:17], vcc
	s_cbranch_execnz .LBB0_1599
.LBB0_1518:
	s_or_b64 exec, exec, s[16:17]
	v_cmp_gt_i32_e32 vcc, s92, v1
	s_and_saveexec_b64 s[16:17], vcc
	s_cbranch_execz .LBB0_1614

; DEVI float bflo(unsigned w) { return __uint_as_float(w << 16); }
; DEVI float bfhi(unsigned w) { return __uint_as_float(w & 0xffff0000u); }
; template <int MODE>
; DEVI void phase_rows(const Params& p, int l, char* smem) {
;     ...
;             for (int e = 0; e < 16; ++e) {
;                 const int r = rke[e];
;                 if (r < cap) {
;                     const int slot = lat ? (b * 256 + r) : (1024 + b * 32 + r);
;                     const bf16_t* yr = ydn + ((size_t)e * MSLOT + slot) * DM;
;                     if (ny == 0) y0 = yr; else if (ny == 1) y1 = yr; else if (ny == 2) y2 = yr; else if (ny == 3) y3 = yr;
;                     else {
; #pragma unroll
;                         for (int i = 0; i < 8; ++i) { const u32x2 w = *(const u32x2*)(yr + i * 256 + lane * 4);
;                             cacc[i * 4] += bflo(w[0]); cacc[i * 4 + 1] += bfhi(w[0]); cacc[i * 4 + 2] += bflo(w[1]); cacc[i * 4 + 3] += bfhi(w[1]); }
;                     }
;                     ++ny;
;                 }
;             }
.LBB0_1533:
	s_or_b64 exec, exec, s[28:29]
	v_add_u32_e32 v116, 1, v116
	s_or_b64 exec, exec, s[16:17]
	v_cmp_gt_i32_e32 vcc, s92, v91
	s_and_saveexec_b64 s[16:17], vcc
	s_cbranch_execnz .LBB0_1615
.LBB0_1534:
	s_or_b64 exec, exec, s[16:17]
	v_cmp_gt_i32_e32 vcc, s92, v90
	s_and_saveexec_b64 s[16:17], vcc
	s_cbranch_execz .LBB0_1630

; DEVI float bflo(unsigned w) { return __uint_as_float(w << 16); }
; DEVI float bfhi(unsigned w) { return __uint_as_float(w & 0xffff0000u); }
; template <int MODE>
; DEVI void phase_rows(const Params& p, int l, char* smem) {
;     ...
;             for (int e = 0; e < 16; ++e) {
;                 const int r = rke[e];
;                 if (r < cap) {
;                     const int slot = lat ? (b * 256 + r) : (1024 + b * 32 + r);
;                     const bf16_t* yr = ydn + ((size_t)e * MSLOT + slot) * DM;
;                     if (ny == 0) y0 = yr; else if (ny == 1) y1 = yr; else if (ny == 2) y2 = yr; else if (ny == 3) y3 = yr;
;                     else {
; #pragma unroll
;                         for (int i = 0; i < 8; ++i) { const u32x2 w = *(const u32x2*)(yr + i * 256 + lane * 4);
;                             cacc[i * 4] += bflo(w[0]); cacc[i * 4 + 1] += bfhi(w[0]); cacc[i * 4 + 2] += bflo(w[1]); cacc[i * 4 + 3] += bfhi(w[1]); }
;                     }
;                     ++ny;
;                 }
;             }
.LBB0_1549:
	s_or_b64 exec, exec, s[28:29]
	v_add_u32_e32 v116, 1, v116
	s_or_b64 exec, exec, s[16:17]
	v_cmp_gt_i32_e32 vcc, s92, v89
	s_and_saveexec_b64 s[16:17], vcc
	s_cbranch_execnz .LBB0_1631
.LBB0_1550:
	s_or_b64 exec, exec, s[16:17]
	v_cmp_gt_i32_e32 vcc, s92, v88
	s_and_saveexec_b64 s[16:17], vcc
	s_cbranch_execz .LBB0_1646

; DEVI float bflo(unsigned w) { return __uint_as_float(w << 16); }
; DEVI float bfhi(unsigned w) { return __uint_as_float(w & 0xffff0000u); }
; template <int MODE>
; DEVI void phase_rows(const Params& p, int l, char* smem) {
;     ...
;             for (int e = 0; e < 16; ++e) {
;                 const int r = rke[e];
;                 if (r < cap) {
;                     const int slot = lat ? (b * 256 + r) : (1024 + b * 32 + r);
;                     const bf16_t* yr = ydn + ((size_t)e * MSLOT + slot) * DM;
;                     if (ny == 0) y0 = yr; else if (ny == 1) y1 = yr; else if (ny == 2) y2 = yr; else if (ny == 3) y3 = yr;
;                     else {
; #pragma unroll
;                         for (int i = 0; i < 8; ++i) { const u32x2 w = *(const u32x2*)(yr + i * 256 + lane * 4);
;                             cacc[i * 4] += bflo(w[0]); cacc[i * 4 + 1] += bfhi(w[0]); cacc[i * 4 + 2] += bflo(w[1]); cacc[i * 4 + 3] += bfhi(w[1]); }
;                     }
;                     ++ny;
;                 }
;             }
.LBB0_1565:
	s_or_b64 exec, exec, s[28:29]
	v_add_u32_e32 v116, 1, v116
	s_or_b64 exec, exec, s[16:17]
	v_cmp_gt_i32_e32 vcc, s92, v87
	s_and_saveexec_b64 s[16:17], vcc
	s_cbranch_execnz .LBB0_1647
.LBB0_1566:
	s_or_b64 exec, exec, s[16:17]
	v_cmp_gt_i32_e32 vcc, s92, v86
	s_and_saveexec_b64 s[16:17], vcc
	s_cbranch_execz .LBB0_1662

; DEVI float bflo(unsigned w) { return __uint_as_float(w << 16); }
; DEVI float bfhi(unsigned w) { return __uint_as_float(w & 0xffff0000u); }
; template <int MODE>
; DEVI void phase_rows(const Params& p, int l, char* smem) {
;     ...
;             for (int e = 0; e < 16; ++e) {
;                 const int r = rke[e];
;                 if (r < cap) {
;                     const int slot = lat ? (b * 256 + r) : (1024 + b * 32 + r);
;                     const bf16_t* yr = ydn + ((size_t)e * MSLOT + slot) * DM;
;                     if (ny == 0) y0 = yr; else if (ny == 1) y1 = yr; else if (ny == 2) y2 = yr; else if (ny == 3) y3 = yr;
;                     else {
; #pragma unroll
;                         for (int i = 0; i < 8; ++i) { const u32x2 w = *(const u32x2*)(yr + i * 256 + lane * 4);
;                             cacc[i * 4] += bflo(w[0]); cacc[i * 4 + 1] += bfhi(w[0]); cacc[i * 4 + 2] += bflo(w[1]); cacc[i * 4 + 3] += bfhi(w[1]); }
;                     }
;                     ++ny;
;                 }
;             }
.LBB0_1581:
	s_or_b64 exec, exec, s[28:29]
	v_add_u32_e32 v116, 1, v116
	s_or_b64 exec, exec, s[16:17]
	v_cmp_gt_i32_e32 vcc, s92, v84
	s_and_saveexec_b64 s[16:17], vcc
	s_cbranch_execz .LBB0_1467
	s_branch .LBB0_1663
.LBB0_1582:
	s_or_b64 exec, exec, s[16:17]
	v_cmp_gt_i32_e32 vcc, s92, v94
	s_and_saveexec_b64 s[16:17], vcc
	s_cbranch_execz .LBB0_1502

; DEVI float bflo(unsigned w) { return __uint_as_float(w << 16); }
; DEVI float bfhi(unsigned w) { return __uint_as_float(w & 0xffff0000u); }
; template <int MODE>
; DEVI void phase_rows(const Params& p, int l, char* smem) {
;     ...
;             for (int e = 0; e < 16; ++e) {
;                 const int r = rke[e];
;                 if (r < cap) {
;                     const int slot = lat ? (b * 256 + r) : (1024 + b * 32 + r);
;                     const bf16_t* yr = ydn + ((size_t)e * MSLOT + slot) * DM;
;                     if (ny == 0) y0 = yr; else if (ny == 1) y1 = yr; else if (ny == 2) y2 = yr; else if (ny == 3) y3 = yr;
;                     else {
; #pragma unroll
;                         for (int i = 0; i < 8; ++i) { const u32x2 w = *(const u32x2*)(yr + i * 256 + lane * 4);
;                             cacc[i * 4] += bflo(w[0]); cacc[i * 4 + 1] += bfhi(w[0]); cacc[i * 4 + 2] += bflo(w[1]); cacc[i * 4 + 3] += bfhi(w[1]); }
;                     }
;                     ++ny;
;                 }
;             }
.LBB0_1597:
	s_or_b64 exec, exec, s[28:29]
	v_add_u32_e32 v116, 1, v116
	s_or_b64 exec, exec, s[16:17]
	v_cmp_gt_i32_e32 vcc, s92, v93
	s_and_saveexec_b64 s[16:17], vcc
	s_cbranch_execnz .LBB0_1503
.LBB0_1598:
	s_or_b64 exec, exec, s[16:17]
	v_cmp_gt_i32_e32 vcc, s92, v92
	s_and_saveexec_b64 s[16:17], vcc
	s_cbranch_execz .LBB0_1518

; DEVI float bflo(unsigned w) { return __uint_as_float(w << 16); }
; DEVI float bfhi(unsigned w) { return __uint_as_float(w & 0xffff0000u); }
; template <int MODE>
; DEVI void phase_rows(const Params& p, int l, char* smem) {
;     ...
;             for (int e = 0; e < 16; ++e) {
;                 const int r = rke[e];
;                 if (r < cap) {
;                     const int slot = lat ? (b * 256 + r) : (1024 + b * 32 + r);
;                     const bf16_t* yr = ydn + ((size_t)e * MSLOT + slot) * DM;
;                     if (ny == 0) y0 = yr; else if (ny == 1) y1 = yr; else if (ny == 2) y2 = yr; else if (ny == 3) y3 = yr;
;                     else {
; #pragma unroll
;                         for (int i = 0; i < 8; ++i) { const u32x2 w = *(const u32x2*)(yr + i * 256 + lane * 4);
;                             cacc[i * 4] += bflo(w[0]); cacc[i * 4 + 1] += bfhi(w[0]); cacc[i * 4 + 2] += bflo(w[1]); cacc[i * 4 + 3] += bfhi(w[1]); }
;                     }
;                     ++ny;
;                 }
;             }
.LBB0_1613:
	s_or_b64 exec, exec, s[28:29]
	v_add_u32_e32 v116, 1, v116
	s_or_b64 exec, exec, s[16:17]
	v_cmp_gt_i32_e32 vcc, s92, v1
	s_and_saveexec_b64 s[16:17], vcc
	s_cbranch_execnz .LBB0_1519
.LBB0_1614:
	s_or_b64 exec, exec, s[16:17]
	v_cmp_gt_i32_e32 vcc, s92, v91
	s_and_saveexec_b64 s[16:17], vcc
	s_cbranch_execz .LBB0_1534

; DEVI float bflo(unsigned w) { return __uint_as_float(w << 16); }
; DEVI float bfhi(unsigned w) { return __uint_as_float(w & 0xffff0000u); }
; template <int MODE>
; DEVI void phase_rows(const Params& p, int l, char* smem) {
;     ...
;             for (int e = 0; e < 16; ++e) {
;                 const int r = rke[e];
;                 if (r < cap) {
;                     const int slot = lat ? (b * 256 + r) : (1024 + b * 32 + r);
;                     const bf16_t* yr = ydn + ((size_t)e * MSLOT + slot) * DM;
;                     if (ny == 0) y0 = yr; else if (ny == 1) y1 = yr; else if (ny == 2) y2 = yr; else if (ny == 3) y3 = yr;
;                     else {
; #pragma unroll
;                         for (int i = 0; i < 8; ++i) { const u32x2 w = *(const u32x2*)(yr + i * 256 + lane * 4);
;                             cacc[i * 4] += bflo(w[0]); cacc[i * 4 + 1] += bfhi(w[0]); cacc[i * 4 + 2] += bflo(w[1]); cacc[i * 4 + 3] += bfhi(w[1]); }
;                     }
;                     ++ny;
;                 }
;             }
.LBB0_1629:
	s_or_b64 exec, exec, s[28:29]
	v_add_u32_e32 v116, 1, v116
	s_or_b64 exec, exec, s[16:17]
	v_cmp_gt_i32_e32 vcc, s92, v90
	s_and_saveexec_b64 s[16:17], vcc
	s_cbranch_execnz .LBB0_1535
.LBB0_1630:
	s_or_b64 exec, exec, s[16:17]
	v_cmp_gt_i32_e32 vcc, s92, v89
	s_and_saveexec_b64 s[16:17], vcc
	s_cbranch_execz .LBB0_1550

; DEVI float bflo(unsigned w) { return __uint_as_float(w << 16); }
; DEVI float bfhi(unsigned w) { return __uint_as_float(w & 0xffff0000u); }
; template <int MODE>
; DEVI void phase_rows(const Params& p, int l, char* smem) {
;     ...
;             for (int e = 0; e < 16; ++e) {
;                 const int r = rke[e];
;                 if (r < cap) {
;                     const int slot = lat ? (b * 256 + r) : (1024 + b * 32 + r);
;                     const bf16_t* yr = ydn + ((size_t)e * MSLOT + slot) * DM;
;                     if (ny == 0) y0 = yr; else if (ny == 1) y1 = yr; else if (ny == 2) y2 = yr; else if (ny == 3) y3 = yr;
;                     else {
; #pragma unroll
;                         for (int i = 0; i < 8; ++i) { const u32x2 w = *(const u32x2*)(yr + i * 256 + lane * 4);
;                             cacc[i * 4] += bflo(w[0]); cacc[i * 4 + 1] += bfhi(w[0]); cacc[i * 4 + 2] += bflo(w[1]); cacc[i * 4 + 3] += bfhi(w[1]); }
;                     }
;                     ++ny;
;                 }
;             }
.LBB0_1645:
	s_or_b64 exec, exec, s[28:29]
	v_add_u32_e32 v116, 1, v116
	s_or_b64 exec, exec, s[16:17]
	v_cmp_gt_i32_e32 vcc, s92, v88
	s_and_saveexec_b64 s[16:17], vcc
	s_cbranch_execnz .LBB0_1551
.LBB0_1646:
	s_or_b64 exec, exec, s[16:17]
	v_cmp_gt_i32_e32 vcc, s92, v87
	s_and_saveexec_b64 s[16:17], vcc
	s_cbranch_execz .LBB0_1566

; DEVI float bflo(unsigned w) { return __uint_as_float(w << 16); }
; DEVI float bfhi(unsigned w) { return __uint_as_float(w & 0xffff0000u); }
; template <int MODE>
; DEVI void phase_rows(const Params& p, int l, char* smem) {
;     ...
;             for (int e = 0; e < 16; ++e) {
;                 const int r = rke[e];
;                 if (r < cap) {
;                     const int slot = lat ? (b * 256 + r) : (1024 + b * 32 + r);
;                     const bf16_t* yr = ydn + ((size_t)e * MSLOT + slot) * DM;
;                     if (ny == 0) y0 = yr; else if (ny == 1) y1 = yr; else if (ny == 2) y2 = yr; else if (ny == 3) y3 = yr;
;                     else {
; #pragma unroll
;                         for (int i = 0; i < 8; ++i) { const u32x2 w = *(const u32x2*)(yr + i * 256 + lane * 4);
;                             cacc[i * 4] += bflo(w[0]); cacc[i * 4 + 1] += bfhi(w[0]); cacc[i * 4 + 2] += bflo(w[1]); cacc[i * 4 + 3] += bfhi(w[1]); }
;                     }
;                     ++ny;
;                 }
;             }
.LBB0_1661:
	s_or_b64 exec, exec, s[28:29]
	v_add_u32_e32 v116, 1, v116
	s_or_b64 exec, exec, s[16:17]
	v_cmp_gt_i32_e32 vcc, s92, v86
	s_and_saveexec_b64 s[16:17], vcc
	s_cbranch_execnz .LBB0_1567
.LBB0_1662:
	s_or_b64 exec, exec, s[16:17]
	v_cmp_gt_i32_e32 vcc, s92, v84
	s_and_saveexec_b64 s[16:17], vcc
	s_cbranch_execz .LBB0_1467
